# attention unit loops: next unit index requested right after publishing the current one (dequeue atomic latency hidden behind the unit body)
# speedup vs baseline: 1.0572x; 1.0031x over previous
.LBB0_292:
	v_add_u32_e32 v2, v2, v3
	v_add_u32_e32 v2, v2, v5
	v_add_u32_e32 v2, v2, v4
	v_add_u32_e32 v2, v2, v7
	v_add_u32_e32 v2, v2, v6
	v_add_u32_e32 v2, v2, v9
	v_or_b32_e32 v2, v8, v2
	v_cmp_ne_u32_e32 vcc, 0, v2
	s_and_b64 s[0:1], s[30:31], exec
	s_cselect_b32 s50, 16, 0
	v_cndmask_b32_e64 v2, 0, 1, vcc
	s_mov_b32 s5, s81
	v_readfirstlane_b32 s0, v2
	s_bitcmp1_b32 s0, 0
	s_cselect_b64 s[10:11], -1, 0
	s_xor_b64 s[38:39], s[10:11], -1
	s_lshl_b64 s[0:1], s[4:5], 2
	v_readlane_b32 s2, v254, 42
	s_add_u32 s24, s2, s0
	v_readlane_b32 s2, v254, 43
	s_addc_u32 s25, s2, s1
	s_or_b32 s33, s50, 0x400
	s_barrier
	s_mov_b32 s99, 0
	s_branch .LBB0_306

.LBB0_306:
	s_barrier
	s_and_saveexec_b64 s[34:35], s[44:45]
	s_cbranch_execz .LBB0_310
	s_mov_b64 s[42:43], exec
	v_mbcnt_lo_u32_b32 v2, s42, 0
	v_mbcnt_hi_u32_b32 v2, s43, v2
	v_cmp_eq_u32_e32 vcc, 0, v2
	s_and_saveexec_b64 s[40:41], vcc
	s_cbranch_execz .LBB0_309
	s_cmp_eq_u32 s99, 1
	s_cbranch_scc1 .Lpf_gqa_use
	s_bcnt1_i32_b64 s2, s[42:43]
	v_mov_b32_e32 v3, s2
	global_atomic_add v3, v211, v3, s[24:25] sc0
	s_branch .LBB0_309
.Lpf_gqa_use:
	s_waitcnt vmcnt(0)
	v_mov_b32_e32 v3, v250
.LBB0_309:
	s_or_b64 exec, exec, s[40:41]
	s_waitcnt vmcnt(0)
	v_readfirstlane_b32 s2, v3
	v_mov_b32_e32 v3, s92
	s_nop 0
	v_add_u32_e32 v2, s2, v2
	ds_write_b32 v3, v2
	global_atomic_add v250, v211, v1, s[24:25] sc0
	s_mov_b32 s99, 1

.LBB0_323:
	s_mov_b32 s99, 0
	s_or_b32 s33, s50, 0x500
	s_branch .LBB0_326

.LBB0_326:
	s_waitcnt vmcnt(0)
	s_barrier
	s_and_saveexec_b64 s[34:35], s[44:45]
	s_cbranch_execz .LBB0_330
	s_mov_b64 s[42:43], exec
	v_mbcnt_lo_u32_b32 v2, s42, 0
	v_mbcnt_hi_u32_b32 v2, s43, v2
	v_cmp_eq_u32_e32 vcc, 0, v2
	s_and_saveexec_b64 s[40:41], vcc
	s_cbranch_execz .LBB0_329
	s_cmp_eq_u32 s99, 1
	s_cbranch_scc1 .Lpf_diff_use
	s_bcnt1_i32_b64 s2, s[42:43]
	v_mov_b32_e32 v3, s2
	global_atomic_add v3, v211, v3, s[24:25] offset:256 sc0
	s_branch .LBB0_329

.LBB0_329:
	s_or_b64 exec, exec, s[40:41]
	s_waitcnt vmcnt(0)
	v_readfirstlane_b32 s2, v3
	v_mov_b32_e32 v3, s92
	s_nop 0
	v_add_u32_e32 v2, s2, v2
	ds_write_b32 v3, v2
	global_atomic_add v250, v211, v1, s[24:25] offset:256 sc0
	s_mov_b32 s99, 1
